# MoBA unit: the next-unit pull atomic returns straight into its consumer register; no vmcnt(0) right behind it
# speedup vs baseline: 1.0025x; 1.0025x over previous
; __device__ __forceinline__ void moba_unit(const UnitRef& u, char* lds, int* rowtab, int* cq, float* wscr, int* idx_slot, const int pend_idx, const int wid) {
;     ...
;     for (int t = 0; t < 4; ++t) { const char* vp_ = ROWP(u.V, u.n * 256 + t * 64); const char* kp_ = ROWP(u.K, u.n * 256 + t * 64);
;         kv[t][0] = *(const bf16x8*)(vp_ + loff); kv[t][1] = *(const bf16x8*)(vp_ + 32 * PITCH * 2 + loff);
;         kv[t][2] = *(const bf16x8*)(kp_ + loff); kv[t][3] = *(const bf16x8*)(kp_ + 32 * PITCH * 2 + loff); }
;     if (tid < 32) cq[tid] = (tid > u.n) ? u.cnt[tid] : 0;
; __global__ void __launch_bounds__(NWAVES * 64, 2) mk_fwd(Args args) {
;     ...
;             for (;;) {
;                 const int unit = __builtin_amdgcn_readfirstlane(bc[8]);
;                 if (unit >= NU) break;
;                 int lo = 0, hi = 512;
; #pragma unroll 1
;                 while (hi - lo > 1) { const int mid = (lo + hi) >> 1; if (ist_t[mid] <= unit) lo = mid; else hi = mid; }
;                 const int hn = __builtin_amdgcn_readfirstlane(lo), c = unit - __builtin_amdgcn_readfirstlane(ist_t[hn]);
;                 const int h_ = hn >> 5, n_ = hn & 31;
;                 int pend = NU; if (ftid == 0) pend = (int)__hip_atomic_fetch_add(actr, 1u, __ATOMIC_RELAXED, __HIP_MEMORY_SCOPE_AGENT);
;                 mb::UnitRef u;
;                 u.Q = W_qb + (size_t)h_ * T * 128; u.K = W_kb + (size_t)h_ * T * 128; u.V = W_vb + (size_t)h_ * T * 128;
;                 u.O = W_part + (size_t)unit * 512 * 128; u.ML = W_ml + (size_t)unit * 1024; u.LOC = W_loc + (size_t)h_ * T * 4;
;                 u.seg = W_seg + (size_t)hn * 32 * 256; u.cnt = W_cnt + hn * 32;
;                 u.ab = exp2f(-(float)(h_ + 1) * 0.5f) * (1.0f / mb::SCALE); u.n = n_; u.c = c; u.L = __builtin_amdgcn_readfirstlane(nrow_t[hn]); u.unit512 = unit * 512;
;                 mb::moba_unit(u, ldsg, rowtab, cq, wscr, (int*)(ctl + 10368 + 32), pend, wave);
.LBB0_698:
	s_add_i32 s3, s2, s1
	s_ashr_i32 s3, s3, 1
	s_lshl_b32 s4, s3, 2
	s_add_i32 s4, s4, 0
	s_add_i32 s4, s4, 0x23100
	v_mov_b32_e32 v0, s4
	ds_read_b32 v0, v0
	s_waitcnt lgkmcnt(0)
	v_readfirstlane_b32 s4, v0
	s_cmp_gt_i32 s4, s0
	s_cselect_b32 s1, s3, s1
	s_cselect_b32 s2, s2, s3
	s_sub_i32 s3, s1, s2
	s_cmp_gt_i32 s3, 1
	s_cbranch_scc1 .LBB0_698
	s_lshl_b32 s1, s2, 2
	s_add_i32 s10, s1, 0
	s_add_i32 s1, s10, 0x23100
	v_mov_b32_e32 v0, s1
	ds_read_b32 v0, v0
	v_readlane_b32 s1, v254, 30
	s_waitcnt lgkmcnt(0)
	v_readfirstlane_b32 s16, v0
	v_mov_b32_e32 v68, s1
	s_mov_b64 s[4:5], exec
	v_readlane_b32 s6, v254, 28
	v_readlane_b32 s7, v254, 29
	s_and_b64 s[6:7], s[4:5], s[6:7]
	s_mov_b64 exec, s[6:7]
	s_cbranch_execz .LBB0_703
	s_mov_b64 s[8:9], exec
	v_mbcnt_lo_u32_b32 v0, s8, 0
	v_mbcnt_hi_u32_b32 v0, s9, v0
	v_cmp_eq_u32_e32 vcc, 0, v0
	s_and_saveexec_b64 s[6:7], vcc
	s_cbranch_execz .LBB0_702
	s_bcnt1_i32_b64 s1, s[8:9]
	v_readlane_b32 s8, v253, 17
	v_mov_b32_e32 v1, s1
	v_readlane_b32 s9, v253, 18
	s_nop 4
	global_atomic_add v68, v129, v1, s[8:9] sc0
.LBB0_702:
	s_or_b64 exec, exec, s[6:7]
.LBB0_703:
	s_or_b64 exec, exec, s[4:5]
	s_ashr_i32 s4, s2, 5
	s_ashr_i32 s5, s4, 31
	s_ashr_i32 s3, s2, 31
	s_and_b32 s1, s2, 31
	s_lshl_b64 s[6:7], s[4:5], 21
	v_readlane_b32 s8, v253, 21
	s_add_u32 s11, s8, s6
	v_readlane_b32 s8, v253, 22
	s_addc_u32 s12, s8, s7
	v_readlane_b32 s8, v253, 23
	s_add_u32 s13, s8, s6
	v_readlane_b32 s6, v253, 24
	s_addc_u32 s14, s6, s7
	s_add_i32 s6, s10, 0x22900
	v_mov_b32_e32 v0, s6
	s_lshl_b32 s33, s1, 8
	s_lshl_b32 s8, s1, 16
	ds_read_b32 v65, v0
	v_mbcnt_lo_u32_b32 v66, -1, 0
	v_mbcnt_hi_u32_b32 v66, -1, v66
	s_add_u32 s6, s13, s8
	v_add_u32_e32 v64, s88, v66
	v_lshlrev_b32_e32 v67, 3, v66
	v_ashrrev_i32_e32 v71, 4, v64
	v_and_b32_e32 v72, 0x78, v67
	s_addc_u32 s7, s14, 0
	v_lshlrev_b32_e32 v70, 1, v72
	v_lshlrev_b32_e32 v69, 8, v71
	s_add_u32 s8, s11, s8
	v_or_b32_e32 v128, v69, v70
	s_addc_u32 s9, s12, 0
	v_lshl_add_u64 v[4:5], s[6:7], 0, v[128:129]
	global_load_dwordx4 v[0:3], v128, s[6:7]
	global_load_dwordx4 v[8:11], v128, s[8:9]
	s_or_b32 s6, s33, 64
	v_lshl_add_u64 v[12:13], s[8:9], 0, v[128:129]
	s_lshl_b32 s8, s6, 8
	s_mov_b32 s95, s6
	s_add_u32 s6, s13, s8
	s_addc_u32 s7, s14, 0
	s_add_u32 s8, s11, s8
	v_add_co_u32_e32 v4, vcc, s87, v4
	s_addc_u32 s9, s12, 0
	s_nop 0
	v_addc_co_u32_e32 v5, vcc, 0, v5, vcc
	v_lshl_add_u64 v[20:21], s[6:7], 0, v[128:129]
	global_load_dwordx4 v[16:19], v128, s[6:7]
	global_load_dwordx4 v[24:27], v128, s[8:9]
	s_or_b32 s6, s33, 0x80
	v_add_co_u32_e32 v12, vcc, s87, v12
	v_lshl_add_u64 v[28:29], s[8:9], 0, v[128:129]
	s_lshl_b32 s8, s6, 8
	v_addc_co_u32_e32 v13, vcc, 0, v13, vcc
	v_writelane_b32 v254, s6, 32
	s_add_u32 s6, s13, s8
	v_add_co_u32_e32 v20, vcc, s87, v20
	s_addc_u32 s7, s14, 0
	s_nop 0
	v_addc_co_u32_e32 v21, vcc, 0, v21, vcc
	s_add_u32 s8, s11, s8
	v_add_co_u32_e32 v28, vcc, s87, v28
	s_addc_u32 s9, s12, 0
	s_nop 0
	v_addc_co_u32_e32 v29, vcc, 0, v29, vcc
	v_lshl_add_u64 v[36:37], s[6:7], 0, v[128:129]
	global_load_dwordx4 v[32:35], v128, s[6:7]
	global_load_dwordx4 v[40:43], v128, s[8:9]
	s_or_b32 s6, s33, 0xc0
	v_add_co_u32_e32 v36, vcc, s87, v36
	v_lshl_add_u64 v[44:45], s[8:9], 0, v[128:129]
	s_lshl_b32 s8, s6, 8
	v_addc_co_u32_e32 v37, vcc, 0, v37, vcc
	v_writelane_b32 v254, s6, 33
	s_add_u32 s6, s13, s8
	v_add_co_u32_e32 v44, vcc, s87, v44
	s_addc_u32 s7, s14, 0
	s_nop 0
	v_addc_co_u32_e32 v45, vcc, 0, v45, vcc
	s_add_u32 s8, s11, s8
	v_lshl_add_u64 v[52:53], s[6:7], 0, v[128:129]
	s_addc_u32 s9, s12, 0
	v_add_co_u32_e32 v52, vcc, 0x2000, v52
	v_lshl_add_u64 v[60:61], s[8:9], 0, v[128:129]
	s_nop 0
	v_addc_co_u32_e32 v53, vcc, 0, v53, vcc
	v_add_co_u32_e32 v60, vcc, 0x2000, v60
	global_load_dwordx4 v[4:7], v[4:5], off
	s_nop 0
	v_addc_co_u32_e32 v61, vcc, 0, v61, vcc
	global_load_dwordx4 v[12:15], v[12:13], off
	s_waitcnt lgkmcnt(0)
	v_readfirstlane_b32 s17, v65
	global_load_dwordx4 v[20:23], v[20:21], off
	v_cmp_gt_i32_e32 vcc, 32, v64
	global_load_dwordx4 v[28:31], v[28:29], off
	s_nop 0
	global_load_dwordx4 v[36:39], v[36:37], off
	s_nop 0
	global_load_dwordx4 v[44:47], v[44:45], off
	s_nop 0
	global_load_dwordx4 v[48:51], v128, s[6:7]
	global_load_dwordx4 v[56:59], v128, s[8:9]
	s_nop 0
	global_load_dwordx4 v[52:55], v[52:53], off
	s_nop 0
	global_load_dwordx4 v[60:63], v[60:61], off
	s_and_saveexec_b64 s[6:7], vcc
	s_cbranch_execz .LBB0_707
	v_cmp_lt_i32_e32 vcc, s1, v64
	v_mov_b32_e32 v65, 0
	s_and_saveexec_b64 s[8:9], vcc
	s_cbranch_execz .LBB0_706
	s_lshl_b32 s10, s2, 5
	s_ashr_i32 s11, s10, 31
	s_lshl_b64 s[10:11], s[10:11], 2
	v_readlane_b32 s12, v253, 15
	v_readlane_b32 s13, v253, 16
	s_add_u32 s10, s12, s10
	s_addc_u32 s11, s13, s11
	v_mov_b32_e32 v65, v129
	v_lshl_add_u64 v[74:75], v[64:65], 2, s[10:11]
	global_load_dword v65, v[74:75], off
